# P0 table conversion loads contiguous 1 KiB chunks per instruction and re-lays the packed row through LDS, on top of the previous best
# baseline (speedup 1.0000x reference)
; #define LAS __attribute__((address_space(3)))
; __device__ __forceinline__ void cpt_row(const Params& P, unsigned char* ws, int layer, int r2, int lane, const f4 (&v)[8]) {
;     ...
;             for (int q = 0; q < 4; ++q) { const f4 a = v[4 * j + q]; am = fmaxf(am, fmaxf(fmaxf(fabsf(a.x), fabsf(a.y)), fmaxf(fabsf(a.z), fabsf(a.w)))); ss += (a.x * a.x + a.y * a.y) + (a.z * a.z + a.w * a.w); }
; #pragma unroll
;         for (int o = 1; o < 64; o <<= 1) am = fmaxf(am, __shfl_xor(am, o));
; __device__ __forceinline__ void phase_prologue(const Params& P, unsigned char* ws, LAS unsigned char* lds, int tid, int lane, int wave) {
;     LAS float* scr = (LAS float*)(lds + wave * 8704);
.LBB0_41:
	v_mbcnt_lo_u32_b32 v0, -1, 0
	v_mbcnt_hi_u32_b32 v0, -1, v0
	v_and_b32_e32 v1, 64, v0
	v_add_u32_e32 v1, 64, v1
	v_xor_b32_e32 v2, 1, v0
	v_cmp_lt_i32_e32 vcc, v2, v1
	s_lshl_b32 s7, s86, 5
	s_lshl_b32 s6, s28, 2
	v_cndmask_b32_e32 v2, v0, v2, vcc
	v_lshlrev_b32_e32 v69, 2, v2
	v_xor_b32_e32 v2, 2, v0
	v_cmp_lt_i32_e32 vcc, v2, v1
	v_writelane_b32 v252, s7, 2
	s_add_i32 s24, s7, s6
	v_cndmask_b32_e32 v2, v0, v2, vcc
	v_lshlrev_b32_e32 v75, 2, v2
	v_xor_b32_e32 v2, 4, v0
	v_cmp_lt_i32_e32 vcc, v2, v1
	s_lshl_b32 s6, s90, 5
	s_mov_b32 s25, 0
	v_cndmask_b32_e32 v2, v0, v2, vcc
	v_lshlrev_b32_e32 v76, 2, v2
	v_xor_b32_e32 v2, 8, v0
	v_cmp_lt_i32_e32 vcc, v2, v1
	s_lshl_b32 s30, s90, 6
	v_writelane_b32 v252, s6, 3
	v_cndmask_b32_e32 v2, v0, v2, vcc
	v_lshlrev_b32_e32 v77, 2, v2
	v_xor_b32_e32 v2, 16, v0
	v_cmp_lt_i32_e32 vcc, v2, v1
	v_mov_b32_e32 v73, 0
	s_waitcnt lgkmcnt(0)
	s_mov_b64 s[8:9], 0x1000
	v_cndmask_b32_e32 v2, v0, v2, vcc
	v_lshlrev_b32_e32 v78, 2, v2
	v_xor_b32_e32 v2, 32, v0
	v_cmp_lt_i32_e32 vcc, v2, v1
	s_movk_i32 s26, 0x1000
	s_mov_b32 s27, 0x40c00000
	v_cndmask_b32_e32 v0, v0, v2, vcc
	v_lshlrev_b32_e32 v79, 2, v0
	s_mov_b32 s28, 0xf800000
	v_mov_b32_e32 v80, 0x260
	s_mov_b32 s29, 0x80808080
	s_mov_b32 s31, s24
	s_mov_b32 s6, s1
	s_lshr_b32 s44, s91, 6
	s_mul_i32 s44, s44, 0x2200
	v_lshrrev_b32_e32 v97, 2, v74
	v_lshl_add_u32 v97, v97, 4, s44
	v_and_b32_e32 v98, 3, v74
	v_lshl_add_u32 v99, v98, 1, v97
	v_lshl_add_u32 v98, v98, 2, v97
	v_lshl_add_u32 v97, v74, 4, s44
	s_branch .LBB0_45

; __device__ __forceinline__ void cpt_row(const Params& P, unsigned char* ws, int layer, int r2, int lane, const f4 (&v)[8]) {
;     ...
;         unsigned char* dst = ws + (tab ? WS_PV : WS_PU) + (size_t)rr * 1024;
;         if (tab) {
;             const float sc = (am > 0.f) ? 6.f / am : 1.f;
;             if (lane == 0) ((float*)(ws + WS_PSC))[row] = (am > 0.f) ? am * (1.f / 6.f) : 1.f;
;             u4 w;
; #pragma unroll
;             for (int j = 0; j < 2; ++j)
; #pragma unroll
;                 for (int h = 0; h < 2; ++h) { unsigned r = 0u; const f4 a0 = v[4 * j + 2 * h], a1 = v[4 * j + 2 * h + 1];
;                     r = __builtin_amdgcn_cvt_scalef32_pk_fp4_f32(r, a0.x * sc, a0.y * sc, 1.0f, 0); r = __builtin_amdgcn_cvt_scalef32_pk_fp4_f32(r, a0.z * sc, a0.w * sc, 1.0f, 1);
;                     r = __builtin_amdgcn_cvt_scalef32_pk_fp4_f32(r, a1.x * sc, a1.y * sc, 1.0f, 2); r = __builtin_amdgcn_cvt_scalef32_pk_fp4_f32(r, a1.z * sc, a1.w * sc, 1.0f, 3);
;                     w[2 * j + h] = r; }
;             *(u4*)(dst + 16 * lane) = w;
;         } else {
;             ss = wave_sum(ss);
;             const float step = (ss > 0.f) ? 0.335f * sqrtf(ss * (1.f / 2048.f)) : 1.f, inv = 1.f / step;
;             if (lane == 0) ((float*)(ws + WS_PSC))[row] = step * (1.f / 32.f);
;             u4 w;
; #pragma unroll
;             for (int q = 0; q < 4; ++q) { const f4 a = v[q], c = v[4 + q];
;                 const int a0 = min(max((int)floorf(a.x * inv + 8.f), 0), 15), a1 = min(max((int)floorf(a.y * inv + 8.f), 0), 15), a2 = min(max((int)floorf(a.z * inv + 8.f), 0), 15), a3 = min(max((int)floorf(a.w * inv + 8.f), 0), 15);
;                 const int c0 = min(max((int)floorf(c.x * inv + 8.f), 0), 15), c1 = min(max((int)floorf(c.y * inv + 8.f), 0), 15), c2 = min(max((int)floorf(c.z * inv + 8.f), 0), 15), c3 = min(max((int)floorf(c.w * inv + 8.f), 0), 15);
;                 w[q] = (unsigned)(a0 | (((c0 - 8) & 15) << 4)) | ((unsigned)(a1 | (((c1 - 8) & 15) << 4)) << 8) | ((unsigned)(a2 | (((c2 - 8) & 15) << 4)) << 16) | ((unsigned)(a3 | (((c3 - 8) & 15) << 4)) << 24); }
;             *(u4*)(dst + 16 * lane) = w;
.LBB0_43:
	s_cmp_eq_u32 s6, 0x1a000000
	s_cselect_b32 s46, 1, 0
	s_add_u32 s6, s18, s6
	s_addc_u32 s7, s19, s7
	s_lshl_b32 s14, s34, 10
	s_add_u32 s6, s6, s14
	s_addc_u32 s7, s7, 0
	v_lshl_add_u64 v[0:1], s[6:7], 0, v[70:71]
	s_cmp_eq_u32 s46, 1
	s_cbranch_scc1 .Lp0u_v_c1
	ds_write_b32 v98, v32
	ds_write_b32 v98, v33 offset:256
	ds_write_b32 v98, v34 offset:512
	ds_write_b32 v98, v35 offset:768
	s_branch .Lp0u_j_c1
.Lp0u_v_c1:
	ds_write_b16 v99, v32
	ds_write_b16_d16_hi v99, v32 offset:256
	ds_write_b16 v99, v33 offset:512
	ds_write_b16_d16_hi v99, v33 offset:768
	ds_write_b16 v99, v34 offset:8
	ds_write_b16_d16_hi v99, v34 offset:264
	ds_write_b16 v99, v35 offset:520
	ds_write_b16_d16_hi v99, v35 offset:776
.Lp0u_j_c1:
	s_waitcnt lgkmcnt(0)
	ds_read_b128 v[32:35], v97
	s_waitcnt lgkmcnt(0)
	global_store_dwordx4 v[0:1], v[32:35], off

; __device__ __forceinline__ void cpt_load(const Params& P, int layer, int r2, int lane, f4 (&v)[8]) {
;     const int tab = r2 >> 14, rr = layer * 16384 + (r2 & 16383); const float* src = P.in[21 + tab] + (size_t)rr * 2048;
; #pragma unroll
;     for (int j = 0; j < 2; ++j)
; #pragma unroll
;         for (int q = 0; q < 4; ++q) v[4 * j + q] = *(const f4*)(src + 1024 * j + 16 * lane + 4 * q);
; }
; __device__ __forceinline__ void cpt_row(const Params& P, unsigned char* ws, int layer, int r2, int lane, const f4 (&v)[8]) {
;     {
;         const int tab = r2 >> 14, rr = layer * 16384 + (r2 & 16383), row = tab * (DEPTH * 16384) + rr;
;         float am = 0.f, ss = 0.f;
; #pragma unroll
;         for (int j = 0; j < 2; ++j)
; #pragma unroll
;             for (int q = 0; q < 4; ++q) { const f4 a = v[4 * j + q]; am = fmaxf(am, fmaxf(fmaxf(fabsf(a.x), fabsf(a.y)), fmaxf(fabsf(a.z), fabsf(a.w)))); ss += (a.x * a.x + a.y * a.y) + (a.z * a.z + a.w * a.w); }
; #pragma unroll
;         for (int o = 1; o < 64; o <<= 1) am = fmaxf(am, __shfl_xor(am, o));
.LBB0_45:
	s_add_i32 s33, s6, s74
	s_cmp_lt_i32 s33, 0x8000
	s_cselect_b64 s[14:15], -1, 0
	s_and_b64 s[20:21], s[14:15], exec
	s_cselect_b32 s7, s33, s6
	s_ashr_i32 s20, s6, 14
	s_ashr_i32 s21, s20, 31
	s_and_b32 s35, s6, 0x3fff
	s_lshl_b64 s[20:21], s[20:21], 3
	s_add_u32 s20, s88, s20
	s_addc_u32 s21, s89, s21
	s_load_dwordx2 s[20:21], s[20:21], 0xa8
	s_lshl_b32 s22, s35, 13
	s_waitcnt lgkmcnt(0)
	s_add_u32 s20, s20, s22
	s_addc_u32 s21, s21, 0
	s_waitcnt vmcnt(8)
	v_lshl_add_u64 v[0:1], s[20:21], 0, v[70:71]
	v_add_co_u32_e32 v2, vcc, s26, v0
	global_load_dwordx4 v[60:63], v70, s[20:21]
	global_load_dwordx4 v[52:55], v70, s[20:21] offset:1024
	global_load_dwordx4 v[44:47], v70, s[20:21] offset:2048
	global_load_dwordx4 v[36:39], v70, s[20:21] offset:3072
	v_addc_co_u32_e32 v3, vcc, 0, v1, vcc
	global_load_dwordx4 v[56:59], v[2:3], off
	v_lshl_add_u64 v[0:1], v[0:1], 0, s[8:9]
	global_load_dwordx4 v[48:51], v[0:1], off offset:1024
	global_load_dwordx4 v[40:43], v[0:1], off offset:2048
	global_load_dwordx4 v[32:35], v[0:1], off offset:3072
	s_ashr_i32 s20, s7, 14
	s_ashr_i32 s21, s20, 31
	s_and_b32 s34, s7, 0x3fff
	s_lshl_b64 s[20:21], s[20:21], 3
	s_add_u32 s20, s88, s20
	s_addc_u32 s21, s89, s21
	s_load_dwordx2 s[20:21], s[20:21], 0xa8
	s_lshl_b32 s7, s34, 13
	s_mov_b64 s[22:23], -1
	s_waitcnt lgkmcnt(0)
	s_add_u32 s20, s20, s7
	s_addc_u32 s21, s21, 0
	s_waitcnt vmcnt(11)
	v_lshl_add_u64 v[4:5], s[20:21], 0, v[70:71]
	v_lshl_add_u64 v[64:65], v[4:5], 0, s[8:9]
	v_add_co_u32_e32 v4, vcc, s26, v4
	global_load_dwordx4 v[0:3], v70, s[20:21] offset:3072
	global_load_dwordx4 v[8:11], v70, s[20:21] offset:2048
	global_load_dwordx4 v[20:23], v70, s[20:21] offset:1024
	global_load_dwordx4 v[28:31], v70, s[20:21]
	v_addc_co_u32_e32 v5, vcc, 0, v5, vcc
	global_load_dwordx4 v[24:27], v[4:5], off
	s_nop 0
	global_load_dwordx4 v[4:7], v[64:65], off offset:3072
	global_load_dwordx4 v[12:15], v[64:65], off offset:2048
	global_load_dwordx4 v[16:19], v[64:65], off offset:1024
	s_and_b32 s7, s31, 0xffff0000
	s_or_b32 s20, s7, s35
	s_cmpk_lt_u32 s6, 0x4000
	s_waitcnt vmcnt(15)
	v_max_f32_e64 v64, |v63|, |v63|
	v_max_f32_e64 v65, |v62|, |v62|
	s_waitcnt vmcnt(14)
	v_max_f32_e64 v66, |v55|, |v55|
	v_max_f32_e64 v67, |v54|, |v54|
	s_waitcnt vmcnt(13)
	v_max_f32_e64 v81, |v47|, |v47|
	v_max_f32_e64 v82, |v46|, |v46|
	s_waitcnt vmcnt(12)
	v_max_f32_e64 v83, |v39|, |v39|
	v_max_f32_e64 v84, |v38|, |v38|
	v_max_f32_e32 v64, v65, v64
	v_max_f32_e32 v65, v67, v66
	v_max_f32_e32 v66, v82, v81
	v_max_f32_e32 v67, v84, v83
	v_max3_f32 v64, |v60|, |v61|, v64
	v_max3_f32 v65, |v52|, |v53|, v65
	s_waitcnt vmcnt(11)
	v_max_f32_e64 v81, |v59|, |v59|
	v_max_f32_e64 v82, |v58|, |v58|
	s_waitcnt vmcnt(10)
	v_max_f32_e64 v83, |v51|, |v51|
	v_max_f32_e64 v84, |v50|, |v50|
	v_max3_f32 v66, |v44|, |v45|, v66
	v_max3_f32 v67, |v36|, |v37|, v67
	s_waitcnt vmcnt(9)
	v_max_f32_e64 v85, |v43|, |v43|
	v_max_f32_e64 v86, |v42|, |v42|
	s_waitcnt vmcnt(8)
	v_max_f32_e64 v87, |v35|, |v35|
	v_max_f32_e64 v88, |v34|, |v34|
	v_max3_f32 v64, v64, 0, v65
	v_max_f32_e32 v65, v82, v81
	v_max_f32_e32 v81, v84, v83
	v_max_f32_e32 v82, v86, v85
	v_max_f32_e32 v83, v88, v87
	v_max3_f32 v64, v64, v66, v67
	v_max3_f32 v65, |v56|, |v57|, v65
	v_max3_f32 v66, |v48|, |v49|, v81
	v_max3_f32 v67, |v40|, |v41|, v82
	v_max3_f32 v81, |v32|, |v33|, v83
	v_max3_f32 v64, v64, v65, v66
	v_max3_f32 v64, v64, v67, v81
	ds_bpermute_b32 v65, v69, v64
	s_waitcnt lgkmcnt(0)
	v_max_f32_e32 v65, v65, v65
	v_max_f32_e32 v64, v64, v65
	ds_bpermute_b32 v65, v75, v64
	s_waitcnt lgkmcnt(0)
	v_max_f32_e32 v65, v65, v65
	v_max_f32_e32 v64, v64, v65
	ds_bpermute_b32 v65, v76, v64
	s_waitcnt lgkmcnt(0)
	v_max_f32_e32 v65, v65, v65
	v_max_f32_e32 v64, v64, v65
	ds_bpermute_b32 v65, v77, v64
	s_waitcnt lgkmcnt(0)
	v_max_f32_e32 v65, v65, v65
	v_max_f32_e32 v64, v64, v65
	ds_bpermute_b32 v65, v78, v64
	s_waitcnt lgkmcnt(0)
	v_max_f32_e32 v65, v65, v65
	v_max_f32_e32 v81, v64, v65
	ds_bpermute_b32 v82, v79, v81
	s_cbranch_scc1 .LBB0_49
	s_waitcnt lgkmcnt(0)
	v_max_f32_e32 v64, v82, v82
	v_max_f32_e32 v65, v81, v81
	v_max_f32_e32 v64, v65, v64
	v_cmp_lt_f32_e64 s[6:7], 0, v64
	s_and_saveexec_b64 s[22:23], s[4:5]
	s_cbranch_execz .LBB0_48
	s_ashr_i32 s21, s20, 31
	s_lshl_b64 s[36:37], s[20:21], 2
	v_mul_f32_e32 v65, 0x3e2aaaab, v64
	s_add_u32 s36, s2, s36
	v_cndmask_b32_e64 v65, 1.0, v65, s[6:7]
	s_addc_u32 s37, s3, s37
	global_store_dword v73, v65, s[36:37]

; __device__ __forceinline__ void cpt_row(const Params& P, unsigned char* ws, int layer, int r2, int lane, const f4 (&v)[8]) {
;     ...
;         unsigned char* dst = ws + (tab ? WS_PV : WS_PU) + (size_t)rr * 1024;
;         if (tab) {
;             const float sc = (am > 0.f) ? 6.f / am : 1.f;
;             if (lane == 0) ((float*)(ws + WS_PSC))[row] = (am > 0.f) ? am * (1.f / 6.f) : 1.f;
;             u4 w;
; #pragma unroll
;             for (int j = 0; j < 2; ++j)
; #pragma unroll
;                 for (int h = 0; h < 2; ++h) { unsigned r = 0u; const f4 a0 = v[4 * j + 2 * h], a1 = v[4 * j + 2 * h + 1];
;                     r = __builtin_amdgcn_cvt_scalef32_pk_fp4_f32(r, a0.x * sc, a0.y * sc, 1.0f, 0); r = __builtin_amdgcn_cvt_scalef32_pk_fp4_f32(r, a0.z * sc, a0.w * sc, 1.0f, 1);
;                     r = __builtin_amdgcn_cvt_scalef32_pk_fp4_f32(r, a1.x * sc, a1.y * sc, 1.0f, 2); r = __builtin_amdgcn_cvt_scalef32_pk_fp4_f32(r, a1.z * sc, a1.w * sc, 1.0f, 3);
;                     w[2 * j + h] = r; }
;             *(u4*)(dst + 16 * lane) = w;
;         } else {
;             ss = wave_sum(ss);
;             const float step = (ss > 0.f) ? 0.335f * sqrtf(ss * (1.f / 2048.f)) : 1.f, inv = 1.f / step;
;             if (lane == 0) ((float*)(ws + WS_PSC))[row] = step * (1.f / 32.f);
;             u4 w;
; #pragma unroll
;             for (int q = 0; q < 4; ++q) { const f4 a = v[q], c = v[4 + q];
;                 const int a0 = min(max((int)floorf(a.x * inv + 8.f), 0), 15), a1 = min(max((int)floorf(a.y * inv + 8.f), 0), 15), a2 = min(max((int)floorf(a.z * inv + 8.f), 0), 15), a3 = min(max((int)floorf(a.w * inv + 8.f), 0), 15);
;                 const int c0 = min(max((int)floorf(c.x * inv + 8.f), 0), 15), c1 = min(max((int)floorf(c.y * inv + 8.f), 0), 15), c2 = min(max((int)floorf(c.z * inv + 8.f), 0), 15), c3 = min(max((int)floorf(c.w * inv + 8.f), 0), 15);
;                 w[q] = (unsigned)(a0 | (((c0 - 8) & 15) << 4)) | ((unsigned)(a1 | (((c1 - 8) & 15) << 4)) << 8) | ((unsigned)(a2 | (((c2 - 8) & 15) << 4)) << 16) | ((unsigned)(a3 | (((c3 - 8) & 15) << 4)) << 24); }
;             *(u4*)(dst + 16 * lane) = w;
.LBB0_53:
	s_cmp_eq_u32 s6, 0x1a000000
	s_cselect_b32 s45, 1, 0
	s_add_u32 s6, s18, s6
	s_addc_u32 s7, s19, s7
	s_lshl_b32 s20, s35, 10
	s_add_u32 s6, s6, s20
	s_addc_u32 s7, s7, 0
	v_lshl_add_u64 v[32:33], s[6:7], 0, v[70:71]
	s_andn2_b64 vcc, exec, s[14:15]
	s_cmp_eq_u32 s45, 1
	s_cbranch_scc1 .Lp0u_v_c0
	ds_write_b32 v98, v64
	ds_write_b32 v98, v65 offset:256
	ds_write_b32 v98, v66 offset:512
	ds_write_b32 v98, v67 offset:768
	s_branch .Lp0u_j_c0
.Lp0u_v_c0:
	ds_write_b16 v99, v64
	ds_write_b16_d16_hi v99, v64 offset:256
	ds_write_b16 v99, v65 offset:512
	ds_write_b16_d16_hi v99, v65 offset:768
	ds_write_b16 v99, v66 offset:8
	ds_write_b16_d16_hi v99, v66 offset:264
	ds_write_b16 v99, v67 offset:520
	ds_write_b16_d16_hi v99, v67 offset:776
.Lp0u_j_c0:
	s_waitcnt lgkmcnt(0)
	ds_read_b128 v[64:67], v97
	s_waitcnt lgkmcnt(0)
	global_store_dwordx4 v[32:33], v[64:67], off
	s_cbranch_vccnz .LBB0_44
	s_waitcnt vmcnt(5)
	v_max_f32_e64 v32, |v31|, |v31|
	v_max_f32_e64 v33, |v30|, |v30|
	v_max_f32_e32 v32, v33, v32
	v_max_f32_e64 v33, |v23|, |v23|
	v_max_f32_e64 v34, |v22|, |v22|
	v_max_f32_e32 v33, v34, v33
	v_max3_f32 v32, |v28|, |v29|, v32
	v_max3_f32 v33, |v20|, |v21|, v33
	v_max3_f32 v32, v32, 0, v33
	v_max_f32_e64 v33, |v11|, |v11|
	v_max_f32_e64 v34, |v10|, |v10|
	v_max_f32_e32 v33, v34, v33
	v_max_f32_e64 v34, |v3|, |v3|
	v_max_f32_e64 v35, |v2|, |v2|
	v_max_f32_e32 v34, v35, v34
	v_max3_f32 v33, |v8|, |v9|, v33
	v_max3_f32 v34, |v0|, |v1|, v34
	v_max3_f32 v32, v32, v33, v34
	s_waitcnt vmcnt(4)
	v_max_f32_e64 v33, |v27|, |v27|
	v_max_f32_e64 v34, |v26|, |v26|
	v_max_f32_e32 v33, v34, v33
	s_waitcnt vmcnt(1)
	v_max_f32_e64 v34, |v19|, |v19|
	v_max_f32_e64 v35, |v18|, |v18|
	v_max_f32_e32 v34, v35, v34
	v_max3_f32 v33, |v24|, |v25|, v33
	v_max3_f32 v34, |v16|, |v17|, v34
	v_max3_f32 v32, v32, v33, v34
	v_max_f32_e64 v33, |v15|, |v15|
	v_max_f32_e64 v34, |v14|, |v14|
	v_max_f32_e32 v33, v34, v33
	v_max_f32_e64 v34, |v7|, |v7|
	v_max_f32_e64 v35, |v6|, |v6|
	v_max_f32_e32 v34, v35, v34
	v_max3_f32 v33, |v12|, |v13|, v33
	v_max3_f32 v34, |v4|, |v5|, v34
	v_max3_f32 v32, v32, v33, v34
	ds_bpermute_b32 v33, v69, v32
	v_readlane_b32 s6, v252, 3
	s_add_i32 s6, s6, s31
	s_and_b32 s6, s6, 0xffff0000
	s_or_b32 s14, s34, s6
	s_waitcnt lgkmcnt(0)
	v_max_f32_e32 v33, v33, v33
	v_max_f32_e32 v32, v32, v33
	ds_bpermute_b32 v33, v75, v32
	s_cmpk_lt_u32 s33, 0x4000
	s_mov_b64 s[20:21], -1
	s_waitcnt lgkmcnt(0)
	v_max_f32_e32 v33, v33, v33
	v_max_f32_e32 v32, v32, v33
	ds_bpermute_b32 v33, v76, v32
	s_waitcnt lgkmcnt(0)
	v_max_f32_e32 v33, v33, v33
	v_max_f32_e32 v32, v32, v33
	ds_bpermute_b32 v33, v77, v32
	s_waitcnt lgkmcnt(0)
	v_max_f32_e32 v33, v33, v33
	v_max_f32_e32 v32, v32, v33
	ds_bpermute_b32 v33, v78, v32
	s_waitcnt lgkmcnt(0)
	v_max_f32_e32 v33, v33, v33
	v_max_f32_e32 v36, v32, v33
	ds_bpermute_b32 v37, v79, v36
	s_cbranch_scc1 .LBB0_58
	s_waitcnt lgkmcnt(0)
	v_max_f32_e32 v32, v37, v37
	v_max_f32_e32 v33, v36, v36
	v_max_f32_e32 v32, v33, v32
	v_cmp_lt_f32_e64 s[6:7], 0, v32
	s_and_saveexec_b64 s[20:21], s[4:5]
	s_cbranch_execz .LBB0_57
	s_ashr_i32 s15, s14, 31
	s_lshl_b64 s[22:23], s[14:15], 2
	v_mul_f32_e32 v33, 0x3e2aaaab, v32
	s_add_u32 s22, s2, s22
	v_cndmask_b32_e64 v33, 1.0, v33, s[6:7]
	s_addc_u32 s23, s3, s23
	global_store_dword v73, v33, s[22:23]

; #define REP(i) for (int rep_ = 0; rep_ < ((PROBE_DUP == (i)) ? 2 : 1); ++rep_)
; __device__ __forceinline__ void convert_peer_tables(const Params& P, unsigned char* ws, int layer, int r_lo, int r_hi, int gw, int NGW, int lane) {
;     for (int r2 = r_lo + gw; r2 < r_hi; r2 += 2 * NGW) { const bool hb = r2 + NGW < r_hi; const int rb = hb ? r2 + NGW : r2;
;         f4 va[8], vb[8]; cpt_load(P, layer, r2, lane, va); cpt_load(P, layer, rb, lane, vb);
;         cpt_row(P, ws, layer, r2, lane, va); if (hb) cpt_row(P, ws, layer, rb, lane, vb); }
; __device__ __forceinline__ void phase_prologue(const Params& P, unsigned char* ws, LAS unsigned char* lds, int tid, int lane, int wave) {
;     ...
;     REP(22) { convert_peer_tables(P, ws, 0, 0, 2 * 16384, gw, NGW, lane);
;         for (int ly = 1; ly < DEPTH; ++ly) convert_peer_tables(P, ws, ly, TAIL_ROWS, 2 * 16384, gw, NGW, lane); }
.LBB0_63:
	s_and_b64 vcc, exec, s[6:7]
	s_cbranch_vccnz .LBB0_62
	v_cmp_lt_i32_e32 vcc, v77, v76
	s_lshl_b32 s38, s33, 14
	s_mov_b32 s39, s31
	s_waitcnt vmcnt(3)
	v_cndmask_b32_e32 v0, v75, v77, vcc
	v_cmp_lt_i32_e32 vcc, v78, v76
	v_lshlrev_b32_e32 v83, 2, v0
	s_mov_b32 s8, s1
	v_cndmask_b32_e32 v0, v75, v78, vcc
	v_cmp_lt_i32_e32 vcc, v79, v76
	v_lshlrev_b32_e32 v84, 2, v0
	s_nop 0
	v_cndmask_b32_e32 v0, v75, v79, vcc
	v_cmp_lt_i32_e32 vcc, v80, v76
	v_lshlrev_b32_e32 v85, 2, v0
	s_nop 0
	v_cndmask_b32_e32 v0, v75, v80, vcc
	v_cmp_lt_i32_e32 vcc, v81, v76
	v_lshlrev_b32_e32 v86, 2, v0
	s_nop 0
	v_cndmask_b32_e32 v0, v75, v81, vcc
	v_cmp_lt_i32_e32 vcc, v82, v76
	v_lshlrev_b32_e32 v87, 2, v0
	s_nop 0
	v_cndmask_b32_e32 v0, v75, v82, vcc
	v_lshlrev_b32_e32 v88, 2, v0
	s_lshr_b32 s44, s91, 6
	s_mul_i32 s44, s44, 0x2200
	v_lshrrev_b32_e32 v97, 2, v74
	v_lshl_add_u32 v97, v97, 4, s44
	v_and_b32_e32 v98, 3, v74
	v_lshl_add_u32 v99, v98, 1, v97
	v_lshl_add_u32 v98, v98, 2, v97
	v_lshl_add_u32 v97, v74, 4, s44
	s_branch .LBB0_68

; __device__ __forceinline__ void cpt_row(const Params& P, unsigned char* ws, int layer, int r2, int lane, const f4 (&v)[8]) {
;     ...
;         unsigned char* dst = ws + (tab ? WS_PV : WS_PU) + (size_t)rr * 1024;
;         if (tab) {
;             const float sc = (am > 0.f) ? 6.f / am : 1.f;
;             if (lane == 0) ((float*)(ws + WS_PSC))[row] = (am > 0.f) ? am * (1.f / 6.f) : 1.f;
;             u4 w;
; #pragma unroll
;             for (int j = 0; j < 2; ++j)
; #pragma unroll
;                 for (int h = 0; h < 2; ++h) { unsigned r = 0u; const f4 a0 = v[4 * j + 2 * h], a1 = v[4 * j + 2 * h + 1];
;                     r = __builtin_amdgcn_cvt_scalef32_pk_fp4_f32(r, a0.x * sc, a0.y * sc, 1.0f, 0); r = __builtin_amdgcn_cvt_scalef32_pk_fp4_f32(r, a0.z * sc, a0.w * sc, 1.0f, 1);
;                     r = __builtin_amdgcn_cvt_scalef32_pk_fp4_f32(r, a1.x * sc, a1.y * sc, 1.0f, 2); r = __builtin_amdgcn_cvt_scalef32_pk_fp4_f32(r, a1.z * sc, a1.w * sc, 1.0f, 3);
;                     w[2 * j + h] = r; }
;             *(u4*)(dst + 16 * lane) = w;
;         } else {
;             ss = wave_sum(ss);
;             const float step = (ss > 0.f) ? 0.335f * sqrtf(ss * (1.f / 2048.f)) : 1.f, inv = 1.f / step;
;             if (lane == 0) ((float*)(ws + WS_PSC))[row] = step * (1.f / 32.f);
;             u4 w;
; #pragma unroll
;             for (int q = 0; q < 4; ++q) { const f4 a = v[q], c = v[4 + q];
;                 const int a0 = min(max((int)floorf(a.x * inv + 8.f), 0), 15), a1 = min(max((int)floorf(a.y * inv + 8.f), 0), 15), a2 = min(max((int)floorf(a.z * inv + 8.f), 0), 15), a3 = min(max((int)floorf(a.w * inv + 8.f), 0), 15);
;                 const int c0 = min(max((int)floorf(c.x * inv + 8.f), 0), 15), c1 = min(max((int)floorf(c.y * inv + 8.f), 0), 15), c2 = min(max((int)floorf(c.z * inv + 8.f), 0), 15), c3 = min(max((int)floorf(c.w * inv + 8.f), 0), 15);
;                 w[q] = (unsigned)(a0 | (((c0 - 8) & 15) << 4)) | ((unsigned)(a1 | (((c1 - 8) & 15) << 4)) << 8) | ((unsigned)(a2 | (((c2 - 8) & 15) << 4)) << 16) | ((unsigned)(a3 | (((c3 - 8) & 15) << 4)) << 24); }
;             *(u4*)(dst + 16 * lane) = w;
.LBB0_66:
	s_cmp_eq_u32 s8, 0x1a000000
	s_cselect_b32 s46, 1, 0
	s_add_u32 s14, s18, s8
	s_addc_u32 s24, s19, s9
	s_lshl_b64 s[8:9], s[22:23], 10
	s_add_u32 s8, s14, s8
	s_addc_u32 s9, s24, s9
	v_lshl_add_u64 v[0:1], s[8:9], 0, v[70:71]
	s_cmp_eq_u32 s46, 1
	s_cbranch_scc1 .Lp0u_v_d1
	ds_write_b32 v98, v32
	ds_write_b32 v98, v33 offset:256
	ds_write_b32 v98, v34 offset:512
	ds_write_b32 v98, v35 offset:768
	s_branch .Lp0u_j_d1

; __device__ __forceinline__ void cpt_load(const Params& P, int layer, int r2, int lane, f4 (&v)[8]) {
;     const int tab = r2 >> 14, rr = layer * 16384 + (r2 & 16383); const float* src = P.in[21 + tab] + (size_t)rr * 2048;
; #pragma unroll
;     for (int j = 0; j < 2; ++j)
; #pragma unroll
;         for (int q = 0; q < 4; ++q) v[4 * j + q] = *(const f4*)(src + 1024 * j + 16 * lane + 4 * q);
; }
; __device__ __forceinline__ void cpt_row(const Params& P, unsigned char* ws, int layer, int r2, int lane, const f4 (&v)[8]) {
;     {
;         const int tab = r2 >> 14, rr = layer * 16384 + (r2 & 16383), row = tab * (DEPTH * 16384) + rr;
;         float am = 0.f, ss = 0.f;
; #pragma unroll
;         for (int j = 0; j < 2; ++j)
; #pragma unroll
;             for (int q = 0; q < 4; ++q) { const f4 a = v[4 * j + q]; am = fmaxf(am, fmaxf(fmaxf(fabsf(a.x), fabsf(a.y)), fmaxf(fabsf(a.z), fabsf(a.w)))); ss += (a.x * a.x + a.y * a.y) + (a.z * a.z + a.w * a.w); }
; #pragma unroll
;         for (int o = 1; o < 64; o <<= 1) am = fmaxf(am, __shfl_xor(am, o));
.LBB0_68:
	s_add_i32 s40, s8, s74
	s_cmp_lt_i32 s40, 0x8000
	s_cselect_b64 s[24:25], -1, 0
	s_and_b64 s[22:23], s[24:25], exec
	s_cselect_b32 s9, s40, s8
	s_ashr_i32 s22, s8, 14
	s_and_b32 s14, s8, 0x3fff
	s_ashr_i32 s23, s22, 31
	s_or_b32 s14, s14, s38
	s_lshl_b64 s[22:23], s[22:23], 3
	s_add_u32 s22, s88, s22
	s_addc_u32 s23, s89, s23
	s_load_dwordx2 s[22:23], s[22:23], 0xa8
	s_lshl_b64 s[26:27], s[14:15], 13
	s_waitcnt lgkmcnt(0)
	s_add_u32 s22, s22, s26
	s_addc_u32 s23, s23, s27
	s_waitcnt vmcnt(3)
	v_lshl_add_u64 v[0:1], s[22:23], 0, v[70:71]
	v_add_co_u32_e32 v2, vcc, s34, v0
	global_load_dwordx4 v[60:63], v70, s[22:23]
	global_load_dwordx4 v[52:55], v70, s[22:23] offset:1024
	global_load_dwordx4 v[44:47], v70, s[22:23] offset:2048
	global_load_dwordx4 v[36:39], v70, s[22:23] offset:3072
	v_addc_co_u32_e32 v3, vcc, 0, v1, vcc
	global_load_dwordx4 v[56:59], v[2:3], off
	v_lshl_add_u64 v[0:1], v[0:1], 0, s[20:21]
	global_load_dwordx4 v[48:51], v[0:1], off offset:1024
	global_load_dwordx4 v[40:43], v[0:1], off offset:2048
	global_load_dwordx4 v[32:35], v[0:1], off offset:3072
	s_ashr_i32 s26, s9, 14
	s_and_b32 s9, s9, 0x3fff
	s_ashr_i32 s27, s26, 31
	s_or_b32 s22, s9, s38
	s_lshl_b64 s[26:27], s[26:27], 3
	s_add_u32 s26, s88, s26
	s_addc_u32 s27, s89, s27
	s_load_dwordx2 s[26:27], s[26:27], 0xa8
	s_mov_b32 s23, s15
	s_lshl_b64 s[28:29], s[22:23], 13
	s_waitcnt lgkmcnt(0)
	s_add_u32 s26, s26, s28
	s_addc_u32 s27, s27, s29
	v_lshl_add_u64 v[0:1], s[26:27], 0, v[70:71]
	s_waitcnt vmcnt(9)
	v_lshl_add_u64 v[16:17], v[0:1], 0, s[20:21]
	v_add_co_u32_e32 v0, vcc, s34, v0
	global_load_dwordx4 v[4:7], v70, s[26:27] offset:3072
	global_load_dwordx4 v[12:15], v70, s[26:27] offset:2048
	global_load_dwordx4 v[20:23], v70, s[26:27] offset:1024
	global_load_dwordx4 v[28:31], v70, s[26:27]
	v_addc_co_u32_e32 v1, vcc, 0, v1, vcc
	global_load_dwordx4 v[24:27], v[0:1], off
	s_nop 0
	global_load_dwordx4 v[0:3], v[16:17], off offset:3072
	global_load_dwordx4 v[8:11], v[16:17], off offset:2048
	s_nop 0
	global_load_dwordx4 v[16:19], v[16:17], off offset:1024
	s_and_b32 s9, s39, 0xffff0000
	s_or_b32 s26, s9, s14
	s_cmpk_lt_u32 s8, 0x4000
	s_mov_b64 s[28:29], -1
	s_waitcnt vmcnt(15)
	v_max_f32_e64 v64, |v63|, |v63|
	v_max_f32_e64 v65, |v62|, |v62|
	s_waitcnt vmcnt(14)
	v_max_f32_e64 v66, |v55|, |v55|
	v_max_f32_e64 v67, |v54|, |v54|
	s_waitcnt vmcnt(13)
	v_max_f32_e64 v89, |v47|, |v47|
	v_max_f32_e64 v90, |v46|, |v46|
	s_waitcnt vmcnt(12)
	v_max_f32_e64 v91, |v39|, |v39|
	v_max_f32_e64 v92, |v38|, |v38|
	v_max_f32_e32 v64, v65, v64
	v_max_f32_e32 v65, v67, v66
	v_max_f32_e32 v66, v90, v89
	v_max_f32_e32 v67, v92, v91
	v_max3_f32 v64, |v60|, |v61|, v64
	v_max3_f32 v65, |v52|, |v53|, v65
	s_waitcnt vmcnt(11)
	v_max_f32_e64 v89, |v59|, |v59|
	v_max_f32_e64 v90, |v58|, |v58|
	s_waitcnt vmcnt(10)
	v_max_f32_e64 v91, |v51|, |v51|
	v_max_f32_e64 v92, |v50|, |v50|
	v_max3_f32 v66, |v44|, |v45|, v66
	v_max3_f32 v67, |v36|, |v37|, v67
	s_waitcnt vmcnt(9)
	v_max_f32_e64 v93, |v43|, |v43|
	v_max_f32_e64 v94, |v42|, |v42|
	s_waitcnt vmcnt(8)
	v_max_f32_e64 v95, |v35|, |v35|
	v_max_f32_e64 v96, |v34|, |v34|
	v_max3_f32 v64, v64, 0, v65
	v_max_f32_e32 v65, v90, v89
	v_max_f32_e32 v89, v92, v91
	v_max_f32_e32 v90, v94, v93
	v_max_f32_e32 v91, v96, v95
	v_max3_f32 v64, v64, v66, v67
	v_max3_f32 v65, |v56|, |v57|, v65
	v_max3_f32 v66, |v48|, |v49|, v89
	v_max3_f32 v67, |v40|, |v41|, v90
	v_max3_f32 v64, v64, v65, v66
	v_max3_f32 v65, |v32|, |v33|, v91
	v_max3_f32 v64, v64, v67, v65
	ds_bpermute_b32 v65, v83, v64
	s_waitcnt lgkmcnt(0)
	v_max_f32_e32 v65, v65, v65
	v_max_f32_e32 v64, v64, v65
	ds_bpermute_b32 v65, v84, v64
	s_waitcnt lgkmcnt(0)
	v_max_f32_e32 v65, v65, v65
	v_max_f32_e32 v64, v64, v65
	ds_bpermute_b32 v65, v85, v64
	s_waitcnt lgkmcnt(0)
	v_max_f32_e32 v65, v65, v65
	v_max_f32_e32 v64, v64, v65
	ds_bpermute_b32 v65, v86, v64
	s_waitcnt lgkmcnt(0)
	v_max_f32_e32 v65, v65, v65
	v_max_f32_e32 v64, v64, v65
	ds_bpermute_b32 v65, v87, v64
	s_waitcnt lgkmcnt(0)
	v_max_f32_e32 v65, v65, v65
	v_max_f32_e32 v89, v64, v65
	ds_bpermute_b32 v90, v88, v89
	s_cbranch_scc1 .LBB0_72
	s_waitcnt lgkmcnt(0)
	v_max_f32_e32 v64, v90, v90
	v_max_f32_e32 v65, v89, v89
	v_max_f32_e32 v64, v65, v64
	v_cmp_lt_f32_e64 s[8:9], 0, v64
	s_and_saveexec_b64 s[28:29], s[4:5]
	s_cbranch_execz .LBB0_71
	s_ashr_i32 s27, s26, 31
	s_lshl_b64 s[42:43], s[26:27], 2
	v_mul_f32_e32 v65, 0x3e2aaaab, v64
	s_add_u32 s42, s2, s42
	v_cndmask_b32_e64 v65, 1.0, v65, s[8:9]
	s_addc_u32 s43, s3, s43
	global_store_dword v73, v65, s[42:43]

; __device__ __forceinline__ void cpt_row(const Params& P, unsigned char* ws, int layer, int r2, int lane, const f4 (&v)[8]) {
;     ...
;         unsigned char* dst = ws + (tab ? WS_PV : WS_PU) + (size_t)rr * 1024;
;         if (tab) {
;             const float sc = (am > 0.f) ? 6.f / am : 1.f;
;             if (lane == 0) ((float*)(ws + WS_PSC))[row] = (am > 0.f) ? am * (1.f / 6.f) : 1.f;
;             u4 w;
; #pragma unroll
;             for (int j = 0; j < 2; ++j)
; #pragma unroll
;                 for (int h = 0; h < 2; ++h) { unsigned r = 0u; const f4 a0 = v[4 * j + 2 * h], a1 = v[4 * j + 2 * h + 1];
;                     r = __builtin_amdgcn_cvt_scalef32_pk_fp4_f32(r, a0.x * sc, a0.y * sc, 1.0f, 0); r = __builtin_amdgcn_cvt_scalef32_pk_fp4_f32(r, a0.z * sc, a0.w * sc, 1.0f, 1);
;                     r = __builtin_amdgcn_cvt_scalef32_pk_fp4_f32(r, a1.x * sc, a1.y * sc, 1.0f, 2); r = __builtin_amdgcn_cvt_scalef32_pk_fp4_f32(r, a1.z * sc, a1.w * sc, 1.0f, 3);
;                     w[2 * j + h] = r; }
;             *(u4*)(dst + 16 * lane) = w;
;         } else {
;             ss = wave_sum(ss);
;             const float step = (ss > 0.f) ? 0.335f * sqrtf(ss * (1.f / 2048.f)) : 1.f, inv = 1.f / step;
;             if (lane == 0) ((float*)(ws + WS_PSC))[row] = step * (1.f / 32.f);
;             u4 w;
; #pragma unroll
;             for (int q = 0; q < 4; ++q) { const f4 a = v[q], c = v[4 + q];
;                 const int a0 = min(max((int)floorf(a.x * inv + 8.f), 0), 15), a1 = min(max((int)floorf(a.y * inv + 8.f), 0), 15), a2 = min(max((int)floorf(a.z * inv + 8.f), 0), 15), a3 = min(max((int)floorf(a.w * inv + 8.f), 0), 15);
;                 const int c0 = min(max((int)floorf(c.x * inv + 8.f), 0), 15), c1 = min(max((int)floorf(c.y * inv + 8.f), 0), 15), c2 = min(max((int)floorf(c.z * inv + 8.f), 0), 15), c3 = min(max((int)floorf(c.w * inv + 8.f), 0), 15);
;                 w[q] = (unsigned)(a0 | (((c0 - 8) & 15) << 4)) | ((unsigned)(a1 | (((c1 - 8) & 15) << 4)) << 8) | ((unsigned)(a2 | (((c2 - 8) & 15) << 4)) << 16) | ((unsigned)(a3 | (((c3 - 8) & 15) << 4)) << 24); }
;             *(u4*)(dst + 16 * lane) = w;
.LBB0_76:
	s_cmp_eq_u32 s8, 0x1a000000
	s_cselect_b32 s45, 1, 0
	s_add_u32 s26, s18, s8
	s_addc_u32 s27, s19, s9
	s_lshl_b64 s[8:9], s[14:15], 10
	s_add_u32 s8, s26, s8
	s_addc_u32 s9, s27, s9
	v_lshl_add_u64 v[32:33], s[8:9], 0, v[70:71]
	s_andn2_b64 vcc, exec, s[24:25]
	s_cmp_eq_u32 s45, 1
	s_cbranch_scc1 .Lp0u_v_d0
	ds_write_b32 v98, v64
	ds_write_b32 v98, v65 offset:256
	ds_write_b32 v98, v66 offset:512
	ds_write_b32 v98, v67 offset:768
	s_branch .Lp0u_j_d0

; __device__ __forceinline__ void cpt_row(const Params& P, unsigned char* ws, int layer, int r2, int lane, const f4 (&v)[8]) {
;     ...
;             for (int q = 0; q < 4; ++q) { const f4 a = v[4 * j + q]; am = fmaxf(am, fmaxf(fmaxf(fabsf(a.x), fabsf(a.y)), fmaxf(fabsf(a.z), fabsf(a.w)))); ss += (a.x * a.x + a.y * a.y) + (a.z * a.z + a.w * a.w); }
; #pragma unroll
;         for (int o = 1; o < 64; o <<= 1) am = fmaxf(am, __shfl_xor(am, o));
;         unsigned char* dst = ws + (tab ? WS_PV : WS_PU) + (size_t)rr * 1024;
;         if (tab) {
;             const float sc = (am > 0.f) ? 6.f / am : 1.f;
;             if (lane == 0) ((float*)(ws + WS_PSC))[row] = (am > 0.f) ? am * (1.f / 6.f) : 1.f;
;             u4 w;
; #pragma unroll
;             for (int j = 0; j < 2; ++j)
; #pragma unroll
;                 for (int h = 0; h < 2; ++h) { unsigned r = 0u; const f4 a0 = v[4 * j + 2 * h], a1 = v[4 * j + 2 * h + 1];
;                     r = __builtin_amdgcn_cvt_scalef32_pk_fp4_f32(r, a0.x * sc, a0.y * sc, 1.0f, 0); r = __builtin_amdgcn_cvt_scalef32_pk_fp4_f32(r, a0.z * sc, a0.w * sc, 1.0f, 1);
;                     r = __builtin_amdgcn_cvt_scalef32_pk_fp4_f32(r, a1.x * sc, a1.y * sc, 1.0f, 2); r = __builtin_amdgcn_cvt_scalef32_pk_fp4_f32(r, a1.z * sc, a1.w * sc, 1.0f, 3);
;                     w[2 * j + h] = r; }
;             *(u4*)(dst + 16 * lane) = w;
;         } else {
;             ss = wave_sum(ss);
;             const float step = (ss > 0.f) ? 0.335f * sqrtf(ss * (1.f / 2048.f)) : 1.f, inv = 1.f / step;
;             if (lane == 0) ((float*)(ws + WS_PSC))[row] = step * (1.f / 32.f);
;             u4 w;
; #pragma unroll
;             for (int q = 0; q < 4; ++q) { const f4 a = v[q], c = v[4 + q];
;                 const int a0 = min(max((int)floorf(a.x * inv + 8.f), 0), 15), a1 = min(max((int)floorf(a.y * inv + 8.f), 0), 15), a2 = min(max((int)floorf(a.z * inv + 8.f), 0), 15), a3 = min(max((int)floorf(a.w * inv + 8.f), 0), 15);
;                 const int c0 = min(max((int)floorf(c.x * inv + 8.f), 0), 15), c1 = min(max((int)floorf(c.y * inv + 8.f), 0), 15), c2 = min(max((int)floorf(c.z * inv + 8.f), 0), 15), c3 = min(max((int)floorf(c.w * inv + 8.f), 0), 15);
.Lp0u_j_d0:
	s_waitcnt lgkmcnt(0)
	ds_read_b128 v[64:67], v97
	s_waitcnt lgkmcnt(0)
	global_store_dwordx4 v[32:33], v[64:67], off
	s_cbranch_vccnz .LBB0_67
	s_waitcnt vmcnt(5)
	v_max_f32_e64 v32, |v31|, |v31|
	v_max_f32_e64 v33, |v30|, |v30|
	v_max_f32_e32 v32, v33, v32
	v_max_f32_e64 v33, |v23|, |v23|
	v_max_f32_e64 v34, |v22|, |v22|
	v_max_f32_e32 v33, v34, v33
	v_max3_f32 v32, |v28|, |v29|, v32
	v_max3_f32 v33, |v20|, |v21|, v33
	v_max3_f32 v32, v32, 0, v33
	v_max_f32_e64 v33, |v15|, |v15|
	v_max_f32_e64 v34, |v14|, |v14|
	v_max_f32_e32 v33, v34, v33
	v_max_f32_e64 v34, |v7|, |v7|
	v_max_f32_e64 v35, |v6|, |v6|
	v_max_f32_e32 v34, v35, v34
	v_max3_f32 v33, |v12|, |v13|, v33
	v_max3_f32 v34, |v4|, |v5|, v34
	v_max3_f32 v32, v32, v33, v34
	s_waitcnt vmcnt(4)
	v_max_f32_e64 v33, |v27|, |v27|
	v_max_f32_e64 v34, |v26|, |v26|
	v_max_f32_e32 v33, v34, v33
	s_waitcnt vmcnt(1)
	v_max_f32_e64 v34, |v19|, |v19|
	v_max_f32_e64 v35, |v18|, |v18|
	v_max_f32_e32 v34, v35, v34
	v_max3_f32 v33, |v24|, |v25|, v33
	v_max3_f32 v34, |v16|, |v17|, v34
	v_max3_f32 v32, v32, v33, v34
	v_max_f32_e64 v33, |v11|, |v11|
	v_max_f32_e64 v34, |v10|, |v10|
	v_max_f32_e32 v33, v34, v33
	v_max_f32_e64 v34, |v3|, |v3|
	v_max_f32_e64 v35, |v2|, |v2|
	v_max_f32_e32 v34, v35, v34
	v_max3_f32 v33, |v8|, |v9|, v33
	v_max3_f32 v34, |v0|, |v1|, v34
	v_max3_f32 v32, v32, v33, v34
	ds_bpermute_b32 v33, v83, v32
	v_readlane_b32 s8, v252, 3
	s_add_i32 s8, s8, s39
	s_and_b32 s8, s8, 0xffff0000
	s_or_b32 s24, s22, s8
	s_waitcnt lgkmcnt(0)
	v_max_f32_e32 v33, v33, v33
	v_max_f32_e32 v32, v32, v33
	ds_bpermute_b32 v33, v84, v32
	s_cmpk_lt_u32 s40, 0x4000
	s_mov_b64 s[26:27], -1
	s_waitcnt lgkmcnt(0)
	v_max_f32_e32 v33, v33, v33
	v_max_f32_e32 v32, v32, v33
	ds_bpermute_b32 v33, v85, v32
	s_waitcnt lgkmcnt(0)
	v_max_f32_e32 v33, v33, v33
	v_max_f32_e32 v32, v32, v33
	ds_bpermute_b32 v33, v86, v32
	s_waitcnt lgkmcnt(0)
	v_max_f32_e32 v33, v33, v33
	v_max_f32_e32 v32, v32, v33
	ds_bpermute_b32 v33, v87, v32
	s_waitcnt lgkmcnt(0)
	v_max_f32_e32 v33, v33, v33
	v_max_f32_e32 v36, v32, v33
	ds_bpermute_b32 v37, v88, v36
	s_cbranch_scc1 .LBB0_81
	s_waitcnt lgkmcnt(0)
	v_max_f32_e32 v32, v37, v37
	v_max_f32_e32 v33, v36, v36
	v_max_f32_e32 v32, v33, v32
	v_cmp_lt_f32_e64 s[8:9], 0, v32
	s_and_saveexec_b64 s[26:27], s[4:5]
	s_cbranch_execz .LBB0_80
	s_ashr_i32 s25, s24, 31
	s_lshl_b64 s[28:29], s[24:25], 2
	v_mul_f32_e32 v33, 0x3e2aaaab, v32
	s_add_u32 s28, s2, s28
	v_cndmask_b32_e64 v33, 1.0, v33, s[8:9]
	s_addc_u32 s29, s3, s29
	global_store_dword v73, v33, s[28:29]
